# wave scans in csr (segment lengths, node counts) and prep (bucket counts) done with DPP row_shr/row_bcast instead of six ds_bpermute round trips each
# speedup vs baseline: 1.0088x; 1.0077x over previous
.LBB0_83:
	s_or_b64 exec, exec, s[4:5]
	s_waitcnt vmcnt(1)
	v_cmp_lt_i32_e64 s[22:23], -1, v15
	v_lshrrev_b32_e32 v50, 4, v15
	s_barrier
	s_and_saveexec_b64 s[0:1], s[22:23]
	v_and_b32_e32 v2, 0xffffffc, v50
	v_mov_b32_e32 v3, 1
	ds_add_u32 v2, v3 offset:12512
	s_or_b64 exec, exec, s[0:1]
	s_waitcnt vmcnt(0)
	v_cmp_lt_i32_e64 s[20:21], -1, v1
	v_lshrrev_b32_e32 v49, 4, v1
	s_and_saveexec_b64 s[0:1], s[20:21]
	v_and_b32_e32 v2, 0xffffffc, v49
	v_mov_b32_e32 v3, 1
	ds_add_u32 v2, v3 offset:12512
	s_or_b64 exec, exec, s[0:1]
	v_cmp_lt_i32_e64 s[18:19], -1, v14
	v_lshrrev_b32_e32 v48, 4, v14
	s_and_saveexec_b64 s[0:1], s[18:19]
	v_and_b32_e32 v2, 0xffffffc, v48
	v_mov_b32_e32 v3, 1
	ds_add_u32 v2, v3 offset:12512
	s_or_b64 exec, exec, s[0:1]
	v_cmp_lt_i32_e64 s[16:17], -1, v17
	v_lshrrev_b32_e32 v47, 4, v17
	s_and_saveexec_b64 s[0:1], s[16:17]
	v_and_b32_e32 v2, 0xffffffc, v47
	v_mov_b32_e32 v3, 1
	ds_add_u32 v2, v3 offset:12512
	s_or_b64 exec, exec, s[0:1]
	v_cmp_lt_i32_e64 s[14:15], -1, v20
	v_lshrrev_b32_e32 v46, 4, v20
	s_and_saveexec_b64 s[0:1], s[14:15]
	v_and_b32_e32 v2, 0xffffffc, v46
	v_mov_b32_e32 v3, 1
	ds_add_u32 v2, v3 offset:12512
	s_or_b64 exec, exec, s[0:1]
	v_cmp_lt_i32_e64 s[12:13], -1, v22
	v_lshrrev_b32_e32 v45, 4, v22
	s_and_saveexec_b64 s[0:1], s[12:13]
	v_and_b32_e32 v2, 0xffffffc, v45
	v_mov_b32_e32 v3, 1
	ds_add_u32 v2, v3 offset:12512
	s_or_b64 exec, exec, s[0:1]
	v_cmp_lt_i32_e64 s[10:11], -1, v24
	v_lshrrev_b32_e32 v44, 4, v24
	s_and_saveexec_b64 s[0:1], s[10:11]
	v_and_b32_e32 v2, 0xffffffc, v44
	v_mov_b32_e32 v3, 1
	ds_add_u32 v2, v3 offset:12512
	s_or_b64 exec, exec, s[0:1]
	v_cmp_lt_i32_e64 s[8:9], -1, v26
	v_lshrrev_b32_e32 v43, 4, v26
	s_and_saveexec_b64 s[0:1], s[8:9]
	v_and_b32_e32 v2, 0xffffffc, v43
	v_mov_b32_e32 v3, 1
	ds_add_u32 v2, v3 offset:12512
	s_or_b64 exec, exec, s[0:1]
	v_cmp_lt_i32_e64 s[6:7], -1, v28
	v_lshrrev_b32_e32 v42, 4, v28
	s_and_saveexec_b64 s[0:1], s[6:7]
	v_and_b32_e32 v2, 0xffffffc, v42
	v_mov_b32_e32 v3, 1
	ds_add_u32 v2, v3 offset:12512
	s_or_b64 exec, exec, s[0:1]
	v_cmp_lt_i32_e64 s[4:5], -1, v30
	v_lshrrev_b32_e32 v41, 4, v30
	s_and_saveexec_b64 s[0:1], s[4:5]
	v_and_b32_e32 v2, 0xffffffc, v41
	v_mov_b32_e32 v3, 1
	ds_add_u32 v2, v3 offset:12512
	s_or_b64 exec, exec, s[0:1]
	v_cmp_lt_i32_e64 s[24:25], -1, v32
	v_lshrrev_b32_e32 v40, 4, v32
	s_and_saveexec_b64 s[0:1], s[24:25]
	v_and_b32_e32 v2, 0xffffffc, v40
	v_mov_b32_e32 v3, 1
	ds_add_u32 v2, v3 offset:12512
	s_or_b64 exec, exec, s[0:1]
	v_cmp_lt_i32_e64 s[0:1], -1, v34
	v_lshrrev_b32_e32 v39, 4, v34
	s_and_saveexec_b64 s[26:27], s[0:1]
	v_and_b32_e32 v2, 0xffffffc, v39
	v_mov_b32_e32 v3, 1
	ds_add_u32 v2, v3 offset:12512
	s_or_b64 exec, exec, s[26:27]
	v_cmp_lt_i32_e32 vcc, -1, v36
	v_lshrrev_b32_e32 v38, 4, v36
	s_and_saveexec_b64 s[26:27], vcc
	v_and_b32_e32 v2, 0xffffffc, v38
	v_mov_b32_e32 v3, 1
	ds_add_u32 v2, v3 offset:12512
	s_or_b64 exec, exec, s[26:27]
	v_lshlrev_b32_e32 v6, 2, v12
	s_waitcnt lgkmcnt(0)
	s_barrier
	ds_read_b128 v[2:5], v6 offset:12512
	v_and_b32_e32 v52, 63, v0
	s_waitcnt lgkmcnt(0)
	v_add_u32_e32 v8, v3, v2
	v_add3_u32 v5, v8, v4, v5
	v_add_u32_e32 v51, 0x30e0, v6
	v_mov_b32_e32 v9, v5
	s_barrier
	s_nop 1
	v_add_u32_dpp v9, v9, v9 row_shr:1 row_mask:0xf bank_mask:0xf
	s_nop 1
	v_add_u32_dpp v9, v9, v9 row_shr:2 row_mask:0xf bank_mask:0xf
	s_nop 1
	v_add_u32_dpp v9, v9, v9 row_shr:4 row_mask:0xf bank_mask:0xf
	s_nop 1
	v_add_u32_dpp v9, v9, v9 row_shr:8 row_mask:0xf bank_mask:0xf
	s_nop 1
	v_add_u32_dpp v9, v9, v9 row_bcast:15 row_mask:0xa bank_mask:0xf
	s_nop 1
	v_add_u32_dpp v9, v9, v9 row_bcast:31 row_mask:0xc bank_mask:0xf
	v_mov_b32_e32 v6, v9
	v_cmp_eq_u32_e64 s[26:27], 63, v52
	s_and_saveexec_b64 s[34:35], s[26:27]
	s_xor_b64 s[26:27], exec, s[34:35]
	v_lshrrev_b32_e32 v7, 4, v0
	v_and_b32_e32 v7, 12, v7
	ds_write_b32 v7, v6 offset:16608
	s_or_b64 exec, exec, s[26:27]
	v_mov_b32_e32 v7, 0
	s_waitcnt lgkmcnt(0)
	s_barrier
	ds_read_b96 v[52:54], v7 offset:16608
	v_cmp_lt_u32_e64 s[26:27], 63, v0
	s_movk_i32 s3, 0x7f
	v_sub_u32_e32 v5, v6, v5
	s_waitcnt lgkmcnt(0)
	v_cndmask_b32_e64 v7, 0, v52, s[26:27]
	v_cmp_lt_u32_e64 s[26:27], s3, v0
	s_movk_i32 s3, 0xbf
	v_add_u32_e32 v5, v7, v5
	v_cndmask_b32_e64 v8, 0, v53, s[26:27]
	v_cmp_lt_u32_e64 s[26:27], s3, v0
	s_movk_i32 s3, 0xc4
	s_nop 0
	v_cndmask_b32_e64 v9, 0, v54, s[26:27]
	v_add3_u32 v6, v5, v8, v9
	v_add_u32_e32 v7, v6, v2
	v_add_u32_e32 v8, v7, v3
	v_add_u32_e32 v9, v8, v4
	v_cmp_gt_u32_e64 s[26:27], s3, v0
	ds_write_b128 v51, v[6:9]
	s_and_saveexec_b64 s[34:35], s[26:27]
	s_cbranch_execz .LBB0_113
	v_lshl_add_u32 v2, v0, 10, s2
	v_ashrrev_i32_e32 v3, 31, v2
	v_lshl_add_u64 v[2:3], v[2:3], 2, s[30:31]
	global_store_dword v[2:3], v6, off

.LBB1_6:
	s_or_b64 exec, exec, s[6:7]
	s_waitcnt vmcnt(0)
	v_sub_u32_e32 v1, v12, v14
	v_and_b32_e32 v5, 63, v0
	v_lshrrev_b32_e32 v38, 4, v0
	v_mov_b32_e32 v2, v1
	s_barrier
	s_nop 1
	v_add_u32_dpp v2, v2, v2 row_shr:1 row_mask:0xf bank_mask:0xf
	s_nop 1
	v_add_u32_dpp v2, v2, v2 row_shr:2 row_mask:0xf bank_mask:0xf
	s_nop 1
	v_add_u32_dpp v2, v2, v2 row_shr:4 row_mask:0xf bank_mask:0xf
	s_nop 1
	v_add_u32_dpp v2, v2, v2 row_shr:8 row_mask:0xf bank_mask:0xf
	s_nop 1
	v_add_u32_dpp v2, v2, v2 row_bcast:15 row_mask:0xa bank_mask:0xf
	s_nop 1
	v_add_u32_dpp v2, v2, v2 row_bcast:31 row_mask:0xc bank_mask:0xf
	v_mov_b32_e32 v22, 0
	v_mov_b32_e32 v23, 0
	v_mov_b32_e32 v24, 0
	v_mov_b32_e32 v25, 0
	v_mov_b32_e32 v26, 0
	v_sub_u32_e32 v10, v2, v1
	v_cmp_eq_u32_e32 vcc, 63, v5
	s_and_saveexec_b64 s[6:7], vcc
	v_add_u32_e32 v2, v26, v2
	v_and_b32_e32 v3, 28, v38
	ds_write_b32 v3, v2 offset:25104
	s_or_b64 exec, exec, s[6:7]
	v_mov_b32_e32 v6, 0
	s_waitcnt lgkmcnt(0)
	s_barrier
	ds_read_b128 v[2:5], v6 offset:25104
	s_load_dwordx4 s[28:31], s[0:1], 0x18
	s_load_dwordx2 s[34:35], s[0:1], 0x28
	ds_read_b128 v[6:9], v6 offset:25120
	s_load_dwordx2 s[36:37], s[0:1], 0x38
	v_cmp_eq_u32_e64 s[6:7], 0, v0
	s_waitcnt lgkmcnt(0)
	v_add_u32_e32 v11, v3, v2
	v_add_u32_e32 v11, v11, v4
	v_add_u32_e32 v11, v11, v5
	v_add_u32_e32 v11, v11, v6
	v_add_u32_e32 v11, v11, v7
	v_add_u32_e32 v11, v11, v8
	v_add_u32_e32 v39, v11, v9
	s_and_saveexec_b64 s[8:9], s[6:7]
	s_cbranch_execz .LBB1_16
	s_movk_i32 s3, 0x800
	v_cmp_lt_i32_e32 vcc, s3, v39
	s_cbranch_vccz .LBB1_13
	s_mov_b64 s[12:13], exec
	v_mbcnt_lo_u32_b32 v11, s12, 0
	v_mbcnt_hi_u32_b32 v11, s13, v11
	v_cmp_eq_u32_e32 vcc, 0, v11
	s_and_saveexec_b64 s[10:11], vcc
	s_cbranch_execz .LBB1_12
	s_load_dwordx2 s[14:15], s[0:1], 0x10
	s_bcnt1_i32_b64 s3, s[12:13]
	v_mul_lo_u32 v15, v39, s3
	v_mov_b32_e32 v21, 0
	s_waitcnt lgkmcnt(0)
	global_atomic_add v15, v21, v15, s[14:15] sc0

.LBB1_63:
	s_or_b64 exec, exec, s[40:41]
	s_waitcnt lgkmcnt(0)
	s_barrier
	s_and_saveexec_b64 s[10:11], s[4:5]
	s_cbranch_execz .LBB1_67
	v_lshlrev_b32_e32 v22, 2, v0
	ds_read_b32 v10, v22 offset:24848
	v_add_u32_e32 v11, 0x6110, v22
	s_waitcnt lgkmcnt(0)
	v_mov_b32_e32 v13, v10
	s_nop 1
	v_add_u32_dpp v13, v13, v13 row_shr:1 row_mask:0xf bank_mask:0xf
	s_nop 1
	v_add_u32_dpp v13, v13, v13 row_shr:2 row_mask:0xf bank_mask:0xf
	s_nop 1
	v_add_u32_dpp v13, v13, v13 row_shr:4 row_mask:0xf bank_mask:0xf
	s_nop 1
	v_add_u32_dpp v13, v13, v13 row_shr:8 row_mask:0xf bank_mask:0xf
	s_nop 1
	v_add_u32_dpp v13, v13, v13 row_bcast:15 row_mask:0xa bank_mask:0xf
	s_nop 1
	v_add_u32_dpp v13, v13, v13 row_bcast:31 row_mask:0xc bank_mask:0xf
	ds_write_b32 v22, v13 offset:24580
	s_and_saveexec_b64 s[4:5], s[6:7]
	v_mov_b32_e32 v16, 0
	ds_write_b32 v16, v16 offset:24576
	s_or_b64 exec, exec, s[4:5]
	v_sub_u32_e32 v10, v13, v10
	ds_write_b32 v11, v10
